# cache policy: nt on the SwiGLU epilogue's act stores (streamed output should not evict GEMM operands from L2)
# baseline (speedup 1.0000x reference)
; __device__ __forceinline__ unsigned cvt_pk_bf16(float lo, float hi) { const f32x2_t v = {lo, hi}; const bf16x2_t b = __builtin_convertvector(v, bf16x2_t); return __builtin_bit_cast(unsigned, b); }
;     __device__ __forceinline__ void operator()(const f32x4 (&acc)[2][2][4][2], const Unit& u, int wr, int wc, int fr, int fq, int ui) const {
;         const int cb = u.pn * BM + wc * 32 + 8 * fq, jcol = u.pn * HALF + wc * 32 + 8 * fq;
;         (void)cb;
;         f32x4 bg[2], bu[2];
;         const float* bt = btab + ui * 256 + wc * 32 + 8 * fq;
; #pragma unroll
;         for (int n = 0; n < 2; ++n) { bg[n] = *(const f32x4*)(bt + 4 * n); bu[n] = *(const f32x4*)(bt + HALF + 4 * n); }
;         float rs[2][4];
; #pragma unroll
;         for (int ai = 0; ai < 2; ++ai)
; #pragma unroll
;             for (int m = 0; m < 4; ++m) rs[ai][m] = rtab[ui * 256 + ai * HALF + wr * 64 + m * 16 + fr];
; #pragma unroll
;         for (int ai = 0; ai < 2; ++ai)
; #pragma unroll
;             for (int m = 0; m < 4; ++m) {
;                 const float r = rs[ai][m]; const int row = u.pm * BM + ai * HALF + wr * 64 + m * 16 + fr;
;                 float g[8], v[8], e[8];
; #pragma unroll
;                 for (int n = 0; n < 2; ++n)
; #pragma unroll
;                     for (int i = 0; i < 4; ++i) { g[n * 4 + i] = fmaf(acc[ai][0][m][n][i], r, bg[n][i]); v[n * 4 + i] = fmaf(acc[ai][1][m][n][i], r, bu[n][i]); }
; #pragma unroll
;                 for (int i = 0; i < 8; ++i) e[i] = __builtin_amdgcn_exp2f(g[i] * (-LOG2E));
; #pragma unroll
;                 for (int i = 0; i < 8; ++i) e[i] = __builtin_amdgcn_rcpf(1.0f + e[i]);
; #pragma unroll
;                 for (int i = 0; i < 8; ++i) e[i] = (g[i] * e[i]) * v[i];
;                 u32x4 w; w.x = cvt_pk_bf16(e[0], e[1]); w.y = cvt_pk_bf16(e[2], e[3]); w.z = cvt_pk_bf16(e[4], e[5]); w.w = cvt_pk_bf16(e[6], e[7]);
;                 *(u32x4*)(act + ((size_t)((row >> 8) * (F / 64) + (jcol >> 6)) * 256 + (row & 255)) * 64 + (jcol & 63)) = w;
.LBB0_249:
	v_lshl_add_u32 v162, s56, 8, v171
	v_lshl_add_u32 v162, v162, 2, 0
	v_lshl_add_u32 v84, s56, 10, v179
	v_add_u32_e32 v162, 0x22000, v162
	ds_read_b128 v[96:99], v84
	ds_read_b128 v[80:83], v84 offset:16
	ds_read_b128 v[100:103], v84 offset:512
	ds_read_b128 v[84:87], v84 offset:528
	ds_read2_b32 v[166:167], v162 offset1:16
	ds_read2_b32 v[176:177], v162 offset0:32 offset1:48
	ds_read2_b32 v[164:165], v162 offset0:128 offset1:144
	ds_read2_b32 v[162:163], v162 offset0:160 offset1:176
	s_lshl_b32 s11, s55, 8
	s_waitcnt lgkmcnt(0)
	v_mov_b32_e32 v222, 0xbfb8aa3b
	v_mov_b32_e32 v224, 1.0
	s_lshl_b32 s9, s57, 7
	s_add_i32 s16, s11, s49
	s_or_b32 s9, s9, s50
	s_ashr_i32 s16, s16, 8
	s_ashr_i32 s9, s9, 6
	s_mulk_i32 s16, 0x58
	s_add_i32 s16, s16, s9
	s_ashr_i32 s17, s16, 31
	s_lshl_b64 s[16:17], s[16:17], 15
	s_add_u32 s16, s16, 0x1000
	s_addc_u32 s17, s17, 0
	v_lshl_add_u64 v[214:215], v[154:155], 0, s[16:17]
	v_lshl_add_u64 v[214:215], v[214:215], 0, v[128:129]
	s_add_i32 s11, s11, s53
	s_ashr_i32 s11, s11, 8
	s_mulk_i32 s11, 0x58
	s_add_i32 s16, s11, s9
	s_ashr_i32 s17, s16, 31
	s_lshl_b64 s[16:17], s[16:17], 15
	s_add_u32 s16, s16, 0x1000
	s_addc_u32 s17, s17, 0
	v_lshl_add_u64 v[216:217], v[156:157], 0, s[16:17]
	v_lshl_add_u64 v[216:217], v[216:217], 0, v[128:129]
	s_mov_b64 s[16:17], -1
	s_movk_i32 s18, 0x1000
	s_mov_b32 s65, s67
	v_pk_fma_f32 v[142:143], v[142:143], v[166:167], v[96:97] op_sel_hi:[1,0,1]
	v_pk_fma_f32 v[144:145], v[144:145], v[166:167], v[98:99] op_sel_hi:[1,0,1]
	v_pk_fma_f32 v[134:135], v[134:135], v[166:167], v[80:81] op_sel_hi:[1,0,1]
	v_pk_fma_f32 v[136:137], v[136:137], v[166:167], v[82:83] op_sel_hi:[1,0,1]
	v_pk_mul_f32 v[198:199], v[142:143], v[222:223] op_sel_hi:[1,0]
	v_pk_mul_f32 v[200:201], v[144:145], v[222:223] op_sel_hi:[1,0]
	v_pk_mul_f32 v[202:203], v[134:135], v[222:223] op_sel_hi:[1,0]
	v_pk_mul_f32 v[204:205], v[136:137], v[222:223] op_sel_hi:[1,0]
	v_pk_fma_f32 v[138:139], v[138:139], v[166:167], v[100:101] op_sel_hi:[1,0,1]
	v_pk_fma_f32 v[140:141], v[140:141], v[166:167], v[102:103] op_sel_hi:[1,0,1]
	v_pk_fma_f32 v[130:131], v[130:131], v[166:167], v[84:85] op_sel_hi:[1,0,1]
	v_pk_fma_f32 v[132:133], v[132:133], v[166:167], v[86:87] op_sel_hi:[1,0,1]
	v_exp_f32_e32 v198, v198
	v_exp_f32_e32 v199, v199
	v_exp_f32_e32 v200, v200
	v_exp_f32_e32 v201, v201
	v_exp_f32_e32 v202, v202
	v_exp_f32_e32 v203, v203
	v_exp_f32_e32 v204, v204
	v_exp_f32_e32 v205, v205
	v_pk_add_f32 v[198:199], v[198:199], v[224:225] op_sel_hi:[1,0]
	v_pk_add_f32 v[200:201], v[200:201], v[224:225] op_sel_hi:[1,0]
	v_pk_add_f32 v[202:203], v[202:203], v[224:225] op_sel_hi:[1,0]
	v_pk_add_f32 v[204:205], v[204:205], v[224:225] op_sel_hi:[1,0]
	v_rcp_f32_e32 v198, v198
	v_rcp_f32_e32 v199, v199
	v_rcp_f32_e32 v200, v200
	v_rcp_f32_e32 v201, v201
	v_rcp_f32_e32 v202, v202
	v_rcp_f32_e32 v203, v203
	v_rcp_f32_e32 v204, v204
	v_rcp_f32_e32 v205, v205
	v_pk_mul_f32 v[142:143], v[142:143], v[198:199]
	v_pk_mul_f32 v[144:145], v[144:145], v[200:201]
	v_pk_mul_f32 v[134:135], v[134:135], v[202:203]
	v_pk_mul_f32 v[136:137], v[136:137], v[204:205]
	v_pk_mul_f32 v[142:143], v[138:139], v[142:143]
	v_pk_mul_f32 v[144:145], v[140:141], v[144:145]
	v_pk_mul_f32 v[134:135], v[130:131], v[134:135]
	v_pk_mul_f32 v[136:137], v[132:133], v[136:137]
	v_cvt_pk_bf16_f32 v206, v142, v143
	v_cvt_pk_bf16_f32 v207, v144, v145
	v_cvt_pk_bf16_f32 v208, v134, v135
	v_cvt_pk_bf16_f32 v209, v136, v137
	global_store_dwordx4 v[214:215], v[206:209], off offset:-4096 nt
	v_pk_fma_f32 v[124:125], v[124:125], v[166:167], v[96:97] op_sel:[0,1,0]
	v_pk_fma_f32 v[126:127], v[126:127], v[166:167], v[98:99] op_sel:[0,1,0]
	v_pk_fma_f32 v[116:117], v[116:117], v[166:167], v[80:81] op_sel:[0,1,0]
	v_pk_fma_f32 v[118:119], v[118:119], v[166:167], v[82:83] op_sel:[0,1,0]
	v_pk_mul_f32 v[198:199], v[124:125], v[222:223] op_sel_hi:[1,0]
	v_pk_mul_f32 v[200:201], v[126:127], v[222:223] op_sel_hi:[1,0]
	v_pk_mul_f32 v[202:203], v[116:117], v[222:223] op_sel_hi:[1,0]
	v_pk_mul_f32 v[204:205], v[118:119], v[222:223] op_sel_hi:[1,0]
	v_pk_fma_f32 v[120:121], v[120:121], v[166:167], v[100:101] op_sel:[0,1,0]
	v_pk_fma_f32 v[122:123], v[122:123], v[166:167], v[102:103] op_sel:[0,1,0]
	v_pk_fma_f32 v[112:113], v[112:113], v[166:167], v[84:85] op_sel:[0,1,0]
	v_pk_fma_f32 v[114:115], v[114:115], v[166:167], v[86:87] op_sel:[0,1,0]
	v_exp_f32_e32 v198, v198
	v_exp_f32_e32 v199, v199
	v_exp_f32_e32 v200, v200
	v_exp_f32_e32 v201, v201
	v_exp_f32_e32 v202, v202
	v_exp_f32_e32 v203, v203
	v_exp_f32_e32 v204, v204
	v_exp_f32_e32 v205, v205
	v_pk_add_f32 v[198:199], v[198:199], v[224:225] op_sel_hi:[1,0]
	v_pk_add_f32 v[200:201], v[200:201], v[224:225] op_sel_hi:[1,0]
	v_pk_add_f32 v[202:203], v[202:203], v[224:225] op_sel_hi:[1,0]
	v_pk_add_f32 v[204:205], v[204:205], v[224:225] op_sel_hi:[1,0]
	v_rcp_f32_e32 v198, v198
	v_rcp_f32_e32 v199, v199
	v_rcp_f32_e32 v200, v200
	v_rcp_f32_e32 v201, v201
	v_rcp_f32_e32 v202, v202
	v_rcp_f32_e32 v203, v203
	v_rcp_f32_e32 v204, v204
	v_rcp_f32_e32 v205, v205
	v_pk_mul_f32 v[124:125], v[124:125], v[198:199]
	v_pk_mul_f32 v[126:127], v[126:127], v[200:201]
	v_pk_mul_f32 v[116:117], v[116:117], v[202:203]
	v_pk_mul_f32 v[118:119], v[118:119], v[204:205]
	v_pk_mul_f32 v[124:125], v[120:121], v[124:125]
	v_pk_mul_f32 v[126:127], v[122:123], v[126:127]
	v_pk_mul_f32 v[116:117], v[112:113], v[116:117]
	v_pk_mul_f32 v[118:119], v[114:115], v[118:119]
	v_cvt_pk_bf16_f32 v210, v124, v125
	v_cvt_pk_bf16_f32 v211, v126, v127
	v_cvt_pk_bf16_f32 v212, v116, v117
	v_cvt_pk_bf16_f32 v213, v118, v119
	global_store_dwordx4 v[214:215], v[210:213], off offset:-2048 nt
; __device__ __forceinline__ unsigned cvt_pk_bf16(float lo, float hi) { const f32x2_t v = {lo, hi}; const bf16x2_t b = __builtin_convertvector(v, bf16x2_t); return __builtin_bit_cast(unsigned, b); }
;     __device__ __forceinline__ void operator()(const f32x4 (&acc)[2][2][4][2], const Unit& u, int wr, int wc, int fr, int fq, int ui) const {
;     ...
;         for (int ai = 0; ai < 2; ++ai)
; #pragma unroll
;             for (int m = 0; m < 4; ++m) {
;                 const float r = rs[ai][m]; const int row = u.pm * BM + ai * HALF + wr * 64 + m * 16 + fr;
;                 float g[8], v[8], e[8];
; #pragma unroll
;                 for (int n = 0; n < 2; ++n)
; #pragma unroll
;                     for (int i = 0; i < 4; ++i) { g[n * 4 + i] = fmaf(acc[ai][0][m][n][i], r, bg[n][i]); v[n * 4 + i] = fmaf(acc[ai][1][m][n][i], r, bu[n][i]); }
; #pragma unroll
;                 for (int i = 0; i < 8; ++i) e[i] = __builtin_amdgcn_exp2f(g[i] * (-LOG2E));
; #pragma unroll
;                 for (int i = 0; i < 8; ++i) e[i] = __builtin_amdgcn_rcpf(1.0f + e[i]);
; #pragma unroll
;                 for (int i = 0; i < 8; ++i) e[i] = (g[i] * e[i]) * v[i];
;                 u32x4 w; w.x = cvt_pk_bf16(e[0], e[1]); w.y = cvt_pk_bf16(e[2], e[3]); w.z = cvt_pk_bf16(e[4], e[5]); w.w = cvt_pk_bf16(e[6], e[7]);
;                 *(u32x4*)(act + ((size_t)((row >> 8) * (F / 64) + (jcol >> 6)) * 256 + (row & 255)) * 64 + (jcol & 63)) = w;
	v_pk_fma_f32 v[108:109], v[108:109], v[176:177], v[96:97] op_sel_hi:[1,0,1]
	v_pk_fma_f32 v[110:111], v[110:111], v[176:177], v[98:99] op_sel_hi:[1,0,1]
	v_pk_fma_f32 v[92:93], v[92:93], v[176:177], v[80:81] op_sel_hi:[1,0,1]
	v_pk_fma_f32 v[94:95], v[94:95], v[176:177], v[82:83] op_sel_hi:[1,0,1]
	v_pk_mul_f32 v[198:199], v[108:109], v[222:223] op_sel_hi:[1,0]
	v_pk_mul_f32 v[200:201], v[110:111], v[222:223] op_sel_hi:[1,0]
	v_pk_mul_f32 v[202:203], v[92:93], v[222:223] op_sel_hi:[1,0]
	v_pk_mul_f32 v[204:205], v[94:95], v[222:223] op_sel_hi:[1,0]
	v_pk_fma_f32 v[104:105], v[104:105], v[176:177], v[100:101] op_sel_hi:[1,0,1]
	v_pk_fma_f32 v[106:107], v[106:107], v[176:177], v[102:103] op_sel_hi:[1,0,1]
	v_pk_fma_f32 v[88:89], v[88:89], v[176:177], v[84:85] op_sel_hi:[1,0,1]
	v_pk_fma_f32 v[90:91], v[90:91], v[176:177], v[86:87] op_sel_hi:[1,0,1]
	v_exp_f32_e32 v198, v198
	v_exp_f32_e32 v199, v199
	v_exp_f32_e32 v200, v200
	v_exp_f32_e32 v201, v201
	v_exp_f32_e32 v202, v202
	v_exp_f32_e32 v203, v203
	v_exp_f32_e32 v204, v204
	v_exp_f32_e32 v205, v205
	v_pk_add_f32 v[198:199], v[198:199], v[224:225] op_sel_hi:[1,0]
	v_pk_add_f32 v[200:201], v[200:201], v[224:225] op_sel_hi:[1,0]
	v_pk_add_f32 v[202:203], v[202:203], v[224:225] op_sel_hi:[1,0]
	v_pk_add_f32 v[204:205], v[204:205], v[224:225] op_sel_hi:[1,0]
	v_rcp_f32_e32 v198, v198
	v_rcp_f32_e32 v199, v199
	v_rcp_f32_e32 v200, v200
	v_rcp_f32_e32 v201, v201
	v_rcp_f32_e32 v202, v202
	v_rcp_f32_e32 v203, v203
	v_rcp_f32_e32 v204, v204
	v_rcp_f32_e32 v205, v205
	v_pk_mul_f32 v[108:109], v[108:109], v[198:199]
	v_pk_mul_f32 v[110:111], v[110:111], v[200:201]
	v_pk_mul_f32 v[92:93], v[92:93], v[202:203]
	v_pk_mul_f32 v[94:95], v[94:95], v[204:205]
	v_pk_mul_f32 v[108:109], v[104:105], v[108:109]
	v_pk_mul_f32 v[110:111], v[106:107], v[110:111]
	v_pk_mul_f32 v[92:93], v[88:89], v[92:93]
	v_pk_mul_f32 v[94:95], v[90:91], v[94:95]
	v_cvt_pk_bf16_f32 v206, v108, v109
	v_cvt_pk_bf16_f32 v207, v110, v111
	v_cvt_pk_bf16_f32 v208, v92, v93
	v_cvt_pk_bf16_f32 v209, v94, v95
	global_store_dwordx4 v[214:215], v[206:209], off nt
	v_pk_fma_f32 v[76:77], v[76:77], v[176:177], v[96:97] op_sel:[0,1,0]
	v_pk_fma_f32 v[78:79], v[78:79], v[176:177], v[98:99] op_sel:[0,1,0]
	v_pk_fma_f32 v[68:69], v[68:69], v[176:177], v[80:81] op_sel:[0,1,0]
	v_pk_fma_f32 v[70:71], v[70:71], v[176:177], v[82:83] op_sel:[0,1,0]
	v_pk_mul_f32 v[198:199], v[76:77], v[222:223] op_sel_hi:[1,0]
	v_pk_mul_f32 v[200:201], v[78:79], v[222:223] op_sel_hi:[1,0]
	v_pk_mul_f32 v[202:203], v[68:69], v[222:223] op_sel_hi:[1,0]
	v_pk_mul_f32 v[204:205], v[70:71], v[222:223] op_sel_hi:[1,0]
	v_pk_fma_f32 v[72:73], v[72:73], v[176:177], v[100:101] op_sel:[0,1,0]
	v_pk_fma_f32 v[74:75], v[74:75], v[176:177], v[102:103] op_sel:[0,1,0]
	v_pk_fma_f32 v[64:65], v[64:65], v[176:177], v[84:85] op_sel:[0,1,0]
	v_pk_fma_f32 v[66:67], v[66:67], v[176:177], v[86:87] op_sel:[0,1,0]
	v_exp_f32_e32 v198, v198
	v_exp_f32_e32 v199, v199
	v_exp_f32_e32 v200, v200
	v_exp_f32_e32 v201, v201
	v_exp_f32_e32 v202, v202
	v_exp_f32_e32 v203, v203
	v_exp_f32_e32 v204, v204
	v_exp_f32_e32 v205, v205
	v_pk_add_f32 v[198:199], v[198:199], v[224:225] op_sel_hi:[1,0]
	v_pk_add_f32 v[200:201], v[200:201], v[224:225] op_sel_hi:[1,0]
	v_pk_add_f32 v[202:203], v[202:203], v[224:225] op_sel_hi:[1,0]
	v_pk_add_f32 v[204:205], v[204:205], v[224:225] op_sel_hi:[1,0]
	v_rcp_f32_e32 v198, v198
	v_rcp_f32_e32 v199, v199
	v_rcp_f32_e32 v200, v200
	v_rcp_f32_e32 v201, v201
	v_rcp_f32_e32 v202, v202
	v_rcp_f32_e32 v203, v203
	v_rcp_f32_e32 v204, v204
	v_rcp_f32_e32 v205, v205
	v_pk_mul_f32 v[76:77], v[76:77], v[198:199]
	v_pk_mul_f32 v[78:79], v[78:79], v[200:201]
	v_pk_mul_f32 v[68:69], v[68:69], v[202:203]
	v_pk_mul_f32 v[70:71], v[70:71], v[204:205]
	v_pk_mul_f32 v[76:77], v[72:73], v[76:77]
	v_pk_mul_f32 v[78:79], v[74:75], v[78:79]
	v_pk_mul_f32 v[68:69], v[64:65], v[68:69]
	v_pk_mul_f32 v[70:71], v[66:67], v[70:71]
	v_cvt_pk_bf16_f32 v210, v76, v77
	v_cvt_pk_bf16_f32 v211, v78, v79
	v_cvt_pk_bf16_f32 v212, v68, v69
	v_cvt_pk_bf16_f32 v213, v70, v71
	global_store_dwordx4 v[214:215], v[210:213], off offset:2048 nt
	v_pk_fma_f32 v[60:61], v[60:61], v[164:165], v[96:97] op_sel_hi:[1,0,1]
	v_pk_fma_f32 v[62:63], v[62:63], v[164:165], v[98:99] op_sel_hi:[1,0,1]
	v_pk_fma_f32 v[52:53], v[52:53], v[164:165], v[80:81] op_sel_hi:[1,0,1]
	v_pk_fma_f32 v[54:55], v[54:55], v[164:165], v[82:83] op_sel_hi:[1,0,1]
	v_pk_mul_f32 v[198:199], v[60:61], v[222:223] op_sel_hi:[1,0]
	v_pk_mul_f32 v[200:201], v[62:63], v[222:223] op_sel_hi:[1,0]
	v_pk_mul_f32 v[202:203], v[52:53], v[222:223] op_sel_hi:[1,0]
	v_pk_mul_f32 v[204:205], v[54:55], v[222:223] op_sel_hi:[1,0]
	v_pk_fma_f32 v[56:57], v[56:57], v[164:165], v[100:101] op_sel_hi:[1,0,1]
	v_pk_fma_f32 v[58:59], v[58:59], v[164:165], v[102:103] op_sel_hi:[1,0,1]
	v_pk_fma_f32 v[48:49], v[48:49], v[164:165], v[84:85] op_sel_hi:[1,0,1]
	v_pk_fma_f32 v[50:51], v[50:51], v[164:165], v[86:87] op_sel_hi:[1,0,1]
	v_exp_f32_e32 v198, v198
	v_exp_f32_e32 v199, v199
	v_exp_f32_e32 v200, v200
	v_exp_f32_e32 v201, v201
	v_exp_f32_e32 v202, v202
	v_exp_f32_e32 v203, v203
	v_exp_f32_e32 v204, v204
	v_exp_f32_e32 v205, v205
	v_pk_add_f32 v[198:199], v[198:199], v[224:225] op_sel_hi:[1,0]
	v_pk_add_f32 v[200:201], v[200:201], v[224:225] op_sel_hi:[1,0]
	v_pk_add_f32 v[202:203], v[202:203], v[224:225] op_sel_hi:[1,0]
	v_pk_add_f32 v[204:205], v[204:205], v[224:225] op_sel_hi:[1,0]
	v_rcp_f32_e32 v198, v198
	v_rcp_f32_e32 v199, v199
	v_rcp_f32_e32 v200, v200
	v_rcp_f32_e32 v201, v201
	v_rcp_f32_e32 v202, v202
	v_rcp_f32_e32 v203, v203
	v_rcp_f32_e32 v204, v204
; __device__ __forceinline__ unsigned cvt_pk_bf16(float lo, float hi) { const f32x2_t v = {lo, hi}; const bf16x2_t b = __builtin_convertvector(v, bf16x2_t); return __builtin_bit_cast(unsigned, b); }
;     __device__ __forceinline__ void operator()(const f32x4 (&acc)[2][2][4][2], const Unit& u, int wr, int wc, int fr, int fq, int ui) const {
;     ...
;         for (int ai = 0; ai < 2; ++ai)
; #pragma unroll
;             for (int m = 0; m < 4; ++m) {
;                 const float r = rs[ai][m]; const int row = u.pm * BM + ai * HALF + wr * 64 + m * 16 + fr;
;                 float g[8], v[8], e[8];
; #pragma unroll
;                 for (int n = 0; n < 2; ++n)
; #pragma unroll
;                     for (int i = 0; i < 4; ++i) { g[n * 4 + i] = fmaf(acc[ai][0][m][n][i], r, bg[n][i]); v[n * 4 + i] = fmaf(acc[ai][1][m][n][i], r, bu[n][i]); }
; #pragma unroll
;                 for (int i = 0; i < 8; ++i) e[i] = __builtin_amdgcn_exp2f(g[i] * (-LOG2E));
; #pragma unroll
;                 for (int i = 0; i < 8; ++i) e[i] = __builtin_amdgcn_rcpf(1.0f + e[i]);
; #pragma unroll
;                 for (int i = 0; i < 8; ++i) e[i] = (g[i] * e[i]) * v[i];
;                 u32x4 w; w.x = cvt_pk_bf16(e[0], e[1]); w.y = cvt_pk_bf16(e[2], e[3]); w.z = cvt_pk_bf16(e[4], e[5]); w.w = cvt_pk_bf16(e[6], e[7]);
;                 *(u32x4*)(act + ((size_t)((row >> 8) * (F / 64) + (jcol >> 6)) * 256 + (row & 255)) * 64 + (jcol & 63)) = w;
	v_rcp_f32_e32 v205, v205
	v_pk_mul_f32 v[60:61], v[60:61], v[198:199]
	v_pk_mul_f32 v[62:63], v[62:63], v[200:201]
	v_pk_mul_f32 v[52:53], v[52:53], v[202:203]
	v_pk_mul_f32 v[54:55], v[54:55], v[204:205]
	v_pk_mul_f32 v[60:61], v[56:57], v[60:61]
	v_pk_mul_f32 v[62:63], v[58:59], v[62:63]
	v_pk_mul_f32 v[52:53], v[48:49], v[52:53]
	v_pk_mul_f32 v[54:55], v[50:51], v[54:55]
	v_cvt_pk_bf16_f32 v206, v60, v61
	v_cvt_pk_bf16_f32 v207, v62, v63
	v_cvt_pk_bf16_f32 v208, v52, v53
	v_cvt_pk_bf16_f32 v209, v54, v55
	global_store_dwordx4 v[216:217], v[206:209], off offset:-4096 nt
	v_pk_fma_f32 v[44:45], v[44:45], v[164:165], v[96:97] op_sel:[0,1,0]
	v_pk_fma_f32 v[46:47], v[46:47], v[164:165], v[98:99] op_sel:[0,1,0]
	v_pk_fma_f32 v[36:37], v[36:37], v[164:165], v[80:81] op_sel:[0,1,0]
	v_pk_fma_f32 v[38:39], v[38:39], v[164:165], v[82:83] op_sel:[0,1,0]
	v_pk_mul_f32 v[198:199], v[44:45], v[222:223] op_sel_hi:[1,0]
	v_pk_mul_f32 v[200:201], v[46:47], v[222:223] op_sel_hi:[1,0]
	v_pk_mul_f32 v[202:203], v[36:37], v[222:223] op_sel_hi:[1,0]
	v_pk_mul_f32 v[204:205], v[38:39], v[222:223] op_sel_hi:[1,0]
	v_pk_fma_f32 v[40:41], v[40:41], v[164:165], v[100:101] op_sel:[0,1,0]
	v_pk_fma_f32 v[42:43], v[42:43], v[164:165], v[102:103] op_sel:[0,1,0]
	v_pk_fma_f32 v[32:33], v[32:33], v[164:165], v[84:85] op_sel:[0,1,0]
	v_pk_fma_f32 v[34:35], v[34:35], v[164:165], v[86:87] op_sel:[0,1,0]
	v_exp_f32_e32 v198, v198
	v_exp_f32_e32 v199, v199
	v_exp_f32_e32 v200, v200
	v_exp_f32_e32 v201, v201
	v_exp_f32_e32 v202, v202
	v_exp_f32_e32 v203, v203
	v_exp_f32_e32 v204, v204
	v_exp_f32_e32 v205, v205
	v_pk_add_f32 v[198:199], v[198:199], v[224:225] op_sel_hi:[1,0]
	v_pk_add_f32 v[200:201], v[200:201], v[224:225] op_sel_hi:[1,0]
	v_pk_add_f32 v[202:203], v[202:203], v[224:225] op_sel_hi:[1,0]
	v_pk_add_f32 v[204:205], v[204:205], v[224:225] op_sel_hi:[1,0]
	v_rcp_f32_e32 v198, v198
	v_rcp_f32_e32 v199, v199
	v_rcp_f32_e32 v200, v200
	v_rcp_f32_e32 v201, v201
	v_rcp_f32_e32 v202, v202
	v_rcp_f32_e32 v203, v203
	v_rcp_f32_e32 v204, v204
	v_rcp_f32_e32 v205, v205
	v_pk_mul_f32 v[44:45], v[44:45], v[198:199]
	v_pk_mul_f32 v[46:47], v[46:47], v[200:201]
	v_pk_mul_f32 v[36:37], v[36:37], v[202:203]
	v_pk_mul_f32 v[38:39], v[38:39], v[204:205]
	v_pk_mul_f32 v[44:45], v[40:41], v[44:45]
	v_pk_mul_f32 v[46:47], v[42:43], v[46:47]
	v_pk_mul_f32 v[36:37], v[32:33], v[36:37]
	v_pk_mul_f32 v[38:39], v[34:35], v[38:39]
	v_cvt_pk_bf16_f32 v210, v44, v45
	v_cvt_pk_bf16_f32 v211, v46, v47
	v_cvt_pk_bf16_f32 v212, v36, v37
	v_cvt_pk_bf16_f32 v213, v38, v39
	global_store_dwordx4 v[216:217], v[210:213], off offset:-2048 nt
	v_pk_fma_f32 v[28:29], v[28:29], v[162:163], v[96:97] op_sel_hi:[1,0,1]
	v_pk_fma_f32 v[30:31], v[30:31], v[162:163], v[98:99] op_sel_hi:[1,0,1]
	v_pk_fma_f32 v[20:21], v[20:21], v[162:163], v[80:81] op_sel_hi:[1,0,1]
	v_pk_fma_f32 v[22:23], v[22:23], v[162:163], v[82:83] op_sel_hi:[1,0,1]
	v_pk_mul_f32 v[198:199], v[28:29], v[222:223] op_sel_hi:[1,0]
	v_pk_mul_f32 v[200:201], v[30:31], v[222:223] op_sel_hi:[1,0]
	v_pk_mul_f32 v[202:203], v[20:21], v[222:223] op_sel_hi:[1,0]
	v_pk_mul_f32 v[204:205], v[22:23], v[222:223] op_sel_hi:[1,0]
	v_pk_fma_f32 v[24:25], v[24:25], v[162:163], v[100:101] op_sel_hi:[1,0,1]
	v_pk_fma_f32 v[26:27], v[26:27], v[162:163], v[102:103] op_sel_hi:[1,0,1]
	v_pk_fma_f32 v[16:17], v[16:17], v[162:163], v[84:85] op_sel_hi:[1,0,1]
	v_pk_fma_f32 v[18:19], v[18:19], v[162:163], v[86:87] op_sel_hi:[1,0,1]
	v_exp_f32_e32 v198, v198
	v_exp_f32_e32 v199, v199
	v_exp_f32_e32 v200, v200
	v_exp_f32_e32 v201, v201
	v_exp_f32_e32 v202, v202
	v_exp_f32_e32 v203, v203
	v_exp_f32_e32 v204, v204
	v_exp_f32_e32 v205, v205
	v_pk_add_f32 v[198:199], v[198:199], v[224:225] op_sel_hi:[1,0]
	v_pk_add_f32 v[200:201], v[200:201], v[224:225] op_sel_hi:[1,0]
	v_pk_add_f32 v[202:203], v[202:203], v[224:225] op_sel_hi:[1,0]
	v_pk_add_f32 v[204:205], v[204:205], v[224:225] op_sel_hi:[1,0]
	v_rcp_f32_e32 v198, v198
	v_rcp_f32_e32 v199, v199
	v_rcp_f32_e32 v200, v200
	v_rcp_f32_e32 v201, v201
	v_rcp_f32_e32 v202, v202
	v_rcp_f32_e32 v203, v203
	v_rcp_f32_e32 v204, v204
	v_rcp_f32_e32 v205, v205
	v_pk_mul_f32 v[28:29], v[28:29], v[198:199]
	v_pk_mul_f32 v[30:31], v[30:31], v[200:201]
	v_pk_mul_f32 v[20:21], v[20:21], v[202:203]
	v_pk_mul_f32 v[22:23], v[22:23], v[204:205]
	v_pk_mul_f32 v[28:29], v[24:25], v[28:29]
	v_pk_mul_f32 v[30:31], v[26:27], v[30:31]
	v_pk_mul_f32 v[20:21], v[16:17], v[20:21]
	v_pk_mul_f32 v[22:23], v[18:19], v[22:23]
	v_cvt_pk_bf16_f32 v206, v28, v29
	v_cvt_pk_bf16_f32 v207, v30, v31
	v_cvt_pk_bf16_f32 v208, v20, v21
	v_cvt_pk_bf16_f32 v209, v22, v23
	global_store_dwordx4 v[216:217], v[206:209], off nt
	v_pk_fma_f32 v[12:13], v[12:13], v[162:163], v[96:97] op_sel:[0,1,0]
	v_pk_fma_f32 v[14:15], v[14:15], v[162:163], v[98:99] op_sel:[0,1,0]
	v_pk_fma_f32 v[4:5], v[4:5], v[162:163], v[80:81] op_sel:[0,1,0]
	v_pk_fma_f32 v[6:7], v[6:7], v[162:163], v[82:83] op_sel:[0,1,0]
	v_pk_mul_f32 v[198:199], v[12:13], v[222:223] op_sel_hi:[1,0]
	v_pk_mul_f32 v[200:201], v[14:15], v[222:223] op_sel_hi:[1,0]
	v_pk_mul_f32 v[202:203], v[4:5], v[222:223] op_sel_hi:[1,0]
	v_pk_mul_f32 v[204:205], v[6:7], v[222:223] op_sel_hi:[1,0]
	v_pk_fma_f32 v[8:9], v[8:9], v[162:163], v[100:101] op_sel:[0,1,0]
	v_pk_fma_f32 v[10:11], v[10:11], v[162:163], v[102:103] op_sel:[0,1,0]
	v_pk_fma_f32 v[0:1], v[0:1], v[162:163], v[84:85] op_sel:[0,1,0]
	v_pk_fma_f32 v[2:3], v[2:3], v[162:163], v[86:87] op_sel:[0,1,0]
	v_exp_f32_e32 v198, v198
	v_exp_f32_e32 v199, v199
	v_exp_f32_e32 v200, v200
	v_exp_f32_e32 v201, v201
	v_exp_f32_e32 v202, v202
	v_exp_f32_e32 v203, v203
	v_exp_f32_e32 v204, v204
	v_exp_f32_e32 v205, v205
	v_pk_add_f32 v[198:199], v[198:199], v[224:225] op_sel_hi:[1,0]
	v_pk_add_f32 v[200:201], v[200:201], v[224:225] op_sel_hi:[1,0]
	v_pk_add_f32 v[202:203], v[202:203], v[224:225] op_sel_hi:[1,0]
	v_pk_add_f32 v[204:205], v[204:205], v[224:225] op_sel_hi:[1,0]
	v_rcp_f32_e32 v198, v198
	v_rcp_f32_e32 v199, v199
	v_rcp_f32_e32 v200, v200
	v_rcp_f32_e32 v201, v201
	v_rcp_f32_e32 v202, v202
	v_rcp_f32_e32 v203, v203
	v_rcp_f32_e32 v204, v204
	v_rcp_f32_e32 v205, v205
	v_pk_mul_f32 v[12:13], v[12:13], v[198:199]
	v_pk_mul_f32 v[14:15], v[14:15], v[200:201]
	v_pk_mul_f32 v[4:5], v[4:5], v[202:203]
	v_pk_mul_f32 v[6:7], v[6:7], v[204:205]
	v_pk_mul_f32 v[12:13], v[8:9], v[12:13]
	v_pk_mul_f32 v[14:15], v[10:11], v[14:15]
	v_pk_mul_f32 v[4:5], v[0:1], v[4:5]
	v_pk_mul_f32 v[6:7], v[2:3], v[6:7]
	v_cvt_pk_bf16_f32 v210, v12, v13
	v_cvt_pk_bf16_f32 v211, v14, v15
	v_cvt_pk_bf16_f32 v212, v4, v5
	v_cvt_pk_bf16_f32 v213, v6, v7
	global_store_dwordx4 v[216:217], v[210:213], off offset:2048 nt
	s_andn2_b64 vcc, exec, s[2:3]
	s_cbranch_vccnz .LBB0_242
	s_andn2_b64 vcc, exec, s[4:5]
	s_cbranch_vccnz .LBB0_241
	s_barrier
	s_branch .LBB0_241
